# attention loop: s_setprio 1 from after the 2nd QK MFMA of each step to the step end, s_setprio 0 for the first-half exps and first QK pair (critical-path-first arbitration between the two staggered wa
# baseline (speedup 1.0000x reference)
; __device__ __forceinline__ void finishSM(f32x16& p0, f32x16& p1, float alpha, float& l_reg, v8i& pa) {
; #pragma unroll
;   for (int r = 0; r < 16; ++r) p1[r] = __builtin_amdgcn_exp2f(p1[r]);
;   float ps = 0;
; #pragma unroll
;   for (int r = 0; r < 16; ++r) ps += p0[r];
; #pragma unroll
;   for (int r = 0; r < 16; ++r) ps += p1[r];
;   { auto rr = __builtin_amdgcn_permlane32_swap(__float_as_uint(ps), __float_as_uint(ps), false, false);
;     ps = __uint_as_float(rr[0]) + __uint_as_float(rr[1]); }
;   l_reg = l_reg * alpha + ps;
; #pragma unroll
;   for (int q = 0; q < 4; ++q) { int w0 = pa[q], w1 = pa[4 + q];
;     w0 = __builtin_amdgcn_cvt_pk_fp8_f32(p0[4 * q], p0[4 * q + 1], w0, false); w0 = __builtin_amdgcn_cvt_pk_fp8_f32(p0[4 * q + 2], p0[4 * q + 3], w0, true);
;     w1 = __builtin_amdgcn_cvt_pk_fp8_f32(p1[4 * q], p1[4 * q + 1], w1, false); w1 = __builtin_amdgcn_cvt_pk_fp8_f32(p1[4 * q + 2], p1[4 * q + 3], w1, true);
;     pa[q] = w0; pa[4 + q] = w1; }
; }
; __device__ __forceinline__ void qkt(f32x16& p0, f32x16& p1, const char* Ks, const v8i* qr, int r32, int hi, const f32x16& nm16) {
; #pragma unroll
;   for (int s = 0; s < 3; ++s) { const int c0 = 4 * s + 2 * hi;
;     const v8i a0 = __builtin_shufflevector(*reinterpret_cast<const v4i*>(Ks + k8_off(r32, c0)), *reinterpret_cast<const v4i*>(Ks + k8_off(r32, c0 + 1)), 0, 1, 2, 3, 4, 5, 6, 7);
;     const v8i a1 = __builtin_shufflevector(*reinterpret_cast<const v4i*>(Ks + 32 * DQK + k8_off(r32, c0)), *reinterpret_cast<const v4i*>(Ks + 32 * DQK + k8_off(r32, c0 + 1)), 0, 1, 2, 3, 4, 5, 6, 7);
;     p0 = __builtin_amdgcn_mfma_scale_f32_32x32x64_f8f6f4(a0, qr[s], s == 0 ? nm16 : p0, 0, 0, 0, 0, 0, 0);
;     p1 = __builtin_amdgcn_mfma_scale_f32_32x32x64_f8f6f4(a1, qr[s], s == 0 ? nm16 : p1, 0, 0, 0, 0, 0, 0); }
; }
; __device__ __forceinline__ void pv_d0(f32x16* o, const char* Vs, v8i pa, int r32, int hi) {
; #pragma unroll
;   for (int d0 = 0; d0 < 4; ++d0) { const int row = 32 * d0 + r32, x = (row >> 2) & 3;
;     const v8i vb = __builtin_shufflevector(*reinterpret_cast<const v4i*>(Vs + row * 64 + (((2 * hi) ^ x) << 4)), *reinterpret_cast<const v4i*>(Vs + row * 64 + (((2 * hi + 1) ^ x) << 4)), 0, 1, 2, 3, 4, 5, 6, 7);
;     o[d0] = __builtin_amdgcn_mfma_scale_f32_32x32x64_f8f6f4(pa, vb, o[d0], 0, 0, 0, 0, 0, 0); }
; }
.Lstg_top_l0:
	ds_read_b128 v[98:101], v196 offset:20480
	ds_read_b128 v[102:105], v197 offset:20480
	ds_read_b128 v[206:209], v196 offset:26624
	ds_read_b128 v[210:213], v197 offset:26624
	v_add_f32_e32 v182, 0, v235
	v_add_f32_e32 v182, v236, v182
	s_waitcnt lgkmcnt(0)
	v_mfma_f32_32x32x64_f8f6f4 v[114:129], v[98:105], v[138:145], v[66:81]
	v_add_f32_e32 v182, v233, v182
	v_add_f32_e32 v182, v234, v182
	v_add_f32_e32 v182, v231, v182
	v_add_f32_e32 v182, v232, v182
	v_add_f32_e32 v182, v229, v182
	v_add_f32_e32 v182, v230, v182
	v_add_f32_e32 v182, v227, v182
	v_add_f32_e32 v182, v228, v182
	v_add_f32_e32 v182, v225, v182
	v_add_f32_e32 v182, v226, v182
	v_exp_f32_e32 v82, v82
	v_add_f32_e32 v182, v223, v182
	v_exp_f32_e32 v83, v83
	v_add_f32_e32 v182, v224, v182
	v_exp_f32_e32 v84, v84
	v_mfma_f32_32x32x64_f8f6f4 v[98:113], v[206:213], v[138:145], v[66:81]
	ds_read_b128 v[206:209], v198 offset:20480
	ds_read_b128 v[210:213], v199 offset:20480
	ds_read_b128 v[238:241], v198 offset:26624
	ds_read_b128 v[242:245], v199 offset:26624
	s_setprio 1
	v_add_f32_e32 v182, v221, v182
	v_exp_f32_e32 v85, v85
	v_add_f32_e32 v182, v222, v182
	v_exp_f32_e32 v86, v86
	v_add_f32_e32 v182, v82, v182
	v_exp_f32_e32 v87, v87
	v_add_f32_e32 v182, v83, v182
	v_exp_f32_e32 v88, v88
	v_add_f32_e32 v182, v84, v182
	v_exp_f32_e32 v89, v89
	v_add_f32_e32 v182, v85, v182
	v_exp_f32_e32 v90, v90
	v_add_f32_e32 v182, v86, v182
	v_exp_f32_e32 v91, v91
	s_waitcnt lgkmcnt(0)
	v_mfma_f32_32x32x64_f8f6f4 v[114:129], v[206:213], v[146:153], v[114:129]
	v_add_f32_e32 v182, v87, v182
	v_exp_f32_e32 v92, v92
	v_exp_f32_e32 v94, v94
	v_exp_f32_e32 v95, v95
	v_add_f32_e32 v182, v88, v182
	v_exp_f32_e32 v93, v93
	v_add_f32_e32 v182, v89, v182
	v_add_f32_e32 v182, v90, v182
	v_add_f32_e32 v182, v91, v182
	v_exp_f32_e32 v96, v96
	v_exp_f32_e32 v97, v97
	v_add_f32_e32 v182, v92, v182
	v_cvt_pk_fp8_f32 v130, v235, v236
	v_cvt_pk_fp8_f32 v134, v82, v83
	v_cvt_pk_fp8_f32 v131, v231, v232
	v_mfma_f32_32x32x64_f8f6f4 v[98:113], v[238:245], v[146:153], v[98:113]
	ds_read_b128 v[206:209], v200 offset:20480
	ds_read_b128 v[210:213], v201 offset:20480
	ds_read_b128 v[238:241], v200 offset:26624
	ds_read_b128 v[242:245], v201 offset:26624
	v_cvt_pk_fp8_f32 v135, v86, v87
	v_cvt_pk_fp8_f32 v132, v227, v228
	v_cvt_pk_fp8_f32 v136, v90, v91
	v_cvt_pk_fp8_f32 v133, v223, v224
	v_cvt_pk_fp8_f32 v137, v94, v95
	v_add_f32_e32 v182, v93, v182
	v_add_f32_e32 v182, v94, v182
	v_add_f32_e32 v182, v95, v182
	v_add_f32_e32 v182, v96, v182
	v_cvt_pk_fp8_f32 v130, v233, v234 op_sel:[0,0,1]
	v_cvt_pk_fp8_f32 v134, v84, v85 op_sel:[0,0,1]
	v_cvt_pk_fp8_f32 v131, v229, v230 op_sel:[0,0,1]
	v_cvt_pk_fp8_f32 v135, v88, v89 op_sel:[0,0,1]
	v_cvt_pk_fp8_f32 v132, v225, v226 op_sel:[0,0,1]
	s_waitcnt lgkmcnt(0)
	v_mfma_f32_32x32x64_f8f6f4 v[114:129], v[206:213], v[154:161], v[114:129]
	v_cvt_pk_fp8_f32 v136, v92, v93 op_sel:[0,0,1]
	v_cvt_pk_fp8_f32 v133, v221, v222 op_sel:[0,0,1]
	v_cvt_pk_fp8_f32 v137, v96, v97 op_sel:[0,0,1]
	v_add_f32_e32 v206, v97, v182
	v_mov_b32_e32 v207, v206
	s_nop 1
	v_permlane32_swap_b32_e32 v206, v207
	v_mfma_f32_32x32x64_f8f6f4 v[98:113], v[238:245], v[154:161], v[98:113]
	s_cmp_eq_u32 s94, 0
	s_cbranch_scc0 .Lstg_mid0_l0
	s_waitcnt vmcnt(0)
	s_barrier
	s_mov_b32 m0, s87
	s_nop 0
	global_load_lds_dwordx4 v164, s[24:25]
	s_mov_b32 m0, s89
	s_nop 0
	global_load_lds_dwordx4 v170, s[26:27]
	s_add_u32 s24, s24, 0x3000
	s_addc_u32 s25, s25, 0
	s_add_u32 s26, s26, 64
	s_addc_u32 s27, s27, 0
.Lstg_mid0_l0:
	v_add_u32_e32 v194, v204, v203
	v_add_u32_e32 v193, v204, v202
	ds_read_b128 v[86:89], v194
	ds_read_b128 v[82:85], v193
	ds_read_b128 v[90:93], v193 offset:2048
	ds_read_b128 v[94:97], v194 offset:2048
	s_nop 4
	v_max_f32_e32 v182, v114, v115
	v_max_f32_e32 v183, v114, v114
	s_waitcnt lgkmcnt(0)
	v_mfma_f32_32x32x64_f8f6f4 v[2:17], v[130:137], v[82:89], v[2:17]
	v_max3_f32 v182, v182, v116, v117
	v_max3_f32 v182, v182, v118, v119
	v_max3_f32 v182, v182, v120, v121
	v_max3_f32 v182, v182, v122, v123
	v_max3_f32 v182, v182, v124, v125
	v_max3_f32 v182, v182, v126, v127
	v_max3_f32 v182, v182, v128, v129
	v_max3_f32 v182, v182, v98, v99
	v_mov_b32_e32 v208, 1.0
	v_mfma_f32_32x32x64_f8f6f4 v[50:65], v[130:137], v[90:97], v[50:65]
	ds_read_b128 v[82:85], v193 offset:4096
	ds_read_b128 v[90:93], v193 offset:6144
	ds_read_b128 v[86:89], v194 offset:4096
	ds_read_b128 v[94:97], v194 offset:6144
	s_waitcnt lgkmcnt(0)
	v_mfma_f32_32x32x64_f8f6f4 v[34:49], v[130:137], v[82:89], v[34:49]
	v_max3_f32 v82, v182, v100, v101
	v_max3_f32 v82, v82, v102, v103
	v_max3_f32 v82, v82, v104, v105
	v_max3_f32 v82, v82, v106, v107
	v_max3_f32 v82, v82, v108, v109
	v_max3_f32 v82, v82, v110, v111
	v_max3_f32 v82, v82, v112, v113
	v_mov_b32_e32 v83, v82
	s_nop 1
	v_permlane32_swap_b32_e32 v82, v83
	v_max_f32_e32 v82, v82, v83
	v_cmp_ge_f32_e32 vcc, s85, v82
	s_cmp_eq_u64 vcc, exec
	v_mfma_f32_32x32x64_f8f6f4 v[18:33], v[130:137], v[90:97], v[18:33]
	s_cbranch_scc0 .LBB0_931
	s_setprio 0
	s_branch .LBB0_894

; template <bool FIRST>
; __device__ __forceinline__ void partialSM(f32x16& p0, f32x16& p1, float& m_reg, f32x16& nm16, float& alpha) {
;   float pmax = p0[0];
; #pragma unroll
;   for (int r = 1; r < 16; ++r) pmax = fmaxf(pmax, p0[r]);
; #pragma unroll
;   for (int r = 0; r < 16; ++r) pmax = fmaxf(pmax, p1[r]);
;   { auto rr = __builtin_amdgcn_permlane32_swap(__float_as_uint(pmax), __float_as_uint(pmax), false, false);
;     pmax = fmaxf(__uint_as_float(rr[0]), __uint_as_float(rr[1])); }
;   if (!FIRST && __builtin_expect(__all(pmax <= THR2), 1)) { alpha = 1.f; }
;   else { const float d = FIRST ? pmax : fmaxf(pmax, 0.f);
;     alpha = FIRST ? 1.f : __builtin_amdgcn_exp2f(-d); m_reg += d;
;     const float nm = -m_reg;
; #pragma unroll
;     for (int r = 0; r < 16; ++r) { p0[r] -= d; p1[r] -= d; float t = nm16[r]; asm volatile("v_mov_b32 %0, %1" : "+v"(t) : "v"(nm)); nm16[r] = t; } }
; #pragma unroll
;   for (int r = 0; r < 16; ++r) p0[r] = __builtin_amdgcn_exp2f(p0[r]);
; }
; __device__ __forceinline__ void finishSM(f32x16& p0, f32x16& p1, float alpha, float& l_reg, v8i& pa) {
; #pragma unroll
;   for (int r = 0; r < 16; ++r) p1[r] = __builtin_amdgcn_exp2f(p1[r]);
;   float ps = 0;
; #pragma unroll
;   for (int r = 0; r < 16; ++r) ps += p0[r];
; #pragma unroll
;   for (int r = 0; r < 16; ++r) ps += p1[r];
;   { auto rr = __builtin_amdgcn_permlane32_swap(__float_as_uint(ps), __float_as_uint(ps), false, false);
;     ps = __uint_as_float(rr[0]) + __uint_as_float(rr[1]); }
;   l_reg = l_reg * alpha + ps;
; #pragma unroll
;   for (int q = 0; q < 4; ++q) { int w0 = pa[q], w1 = pa[4 + q];
;     w0 = __builtin_amdgcn_cvt_pk_fp8_f32(p0[4 * q], p0[4 * q + 1], w0, false); w0 = __builtin_amdgcn_cvt_pk_fp8_f32(p0[4 * q + 2], p0[4 * q + 3], w0, true);
;     w1 = __builtin_amdgcn_cvt_pk_fp8_f32(p1[4 * q], p1[4 * q + 1], w1, false); w1 = __builtin_amdgcn_cvt_pk_fp8_f32(p1[4 * q + 2], p1[4 * q + 3], w1, true);
;     pa[q] = w0; pa[4 + q] = w1; }
; }
; __device__ __forceinline__ void qkt(f32x16& p0, f32x16& p1, const char* Ks, const v8i* qr, int r32, int hi, const f32x16& nm16) {
; #pragma unroll
;   for (int s = 0; s < 3; ++s) { const int c0 = 4 * s + 2 * hi;
;     const v8i a0 = __builtin_shufflevector(*reinterpret_cast<const v4i*>(Ks + k8_off(r32, c0)), *reinterpret_cast<const v4i*>(Ks + k8_off(r32, c0 + 1)), 0, 1, 2, 3, 4, 5, 6, 7);
.Lstg_end0_l0:
	v_exp_f32_e32 v182, v114
	v_exp_f32_e32 v183, v115
	v_exp_f32_e32 v184, v116
	v_exp_f32_e32 v185, v117
	v_exp_f32_e32 v226, v118
	v_exp_f32_e32 v227, v119
	v_exp_f32_e32 v228, v120
	v_exp_f32_e32 v229, v121
	v_exp_f32_e32 v230, v122
	v_exp_f32_e32 v231, v123
	v_exp_f32_e32 v232, v124
	v_exp_f32_e32 v233, v125
	v_exp_f32_e32 v234, v126
	v_exp_f32_e32 v235, v127
	v_exp_f32_e32 v236, v128
	v_exp_f32_e32 v237, v129
	ds_read_b128 v[82:85], v196 offset:49152
	ds_read_b128 v[86:89], v197 offset:49152
	ds_read_b128 v[210:213], v196 offset:55296
	ds_read_b128 v[214:217], v197 offset:55296
	v_add_f32_e32 v209, 0, v182
	v_add_f32_e32 v209, v183, v209
	s_waitcnt lgkmcnt(0)
	v_mfma_f32_32x32x64_f8f6f4 v[114:129], v[82:89], v[138:145], v[66:81]
	v_add_f32_e32 v209, v184, v209
	v_add_f32_e32 v209, v185, v209
	v_add_f32_e32 v209, v226, v209
	v_add_f32_e32 v209, v227, v209
	v_add_f32_e32 v209, v228, v209
	v_add_f32_e32 v209, v229, v209
	v_add_f32_e32 v209, v230, v209
	v_add_f32_e32 v209, v231, v209
	v_add_f32_e32 v209, v232, v209
	v_add_f32_e32 v209, v233, v209
	v_exp_f32_e32 v98, v98
	v_add_f32_e32 v209, v234, v209
	v_exp_f32_e32 v99, v99
	v_add_f32_e32 v209, v235, v209
	v_exp_f32_e32 v100, v100
	v_mfma_f32_32x32x64_f8f6f4 v[82:97], v[210:217], v[138:145], v[66:81]
	ds_read_b128 v[210:213], v198 offset:49152
	ds_read_b128 v[214:217], v199 offset:49152
	ds_read_b128 v[218:221], v198 offset:55296
	ds_read_b128 v[222:225], v199 offset:55296
	s_setprio 1
	v_add_f32_e32 v209, v236, v209
	v_exp_f32_e32 v101, v101
	v_add_f32_e32 v209, v237, v209
	v_exp_f32_e32 v102, v102
	v_add_f32_e32 v209, v98, v209
	v_exp_f32_e32 v103, v103
	v_add_f32_e32 v209, v99, v209
	v_exp_f32_e32 v104, v104
	v_add_f32_e32 v209, v100, v209
	v_exp_f32_e32 v105, v105
	v_add_f32_e32 v209, v101, v209
	v_exp_f32_e32 v106, v106
	v_add_f32_e32 v209, v102, v209
	v_exp_f32_e32 v107, v107
	s_waitcnt lgkmcnt(0)
	v_mfma_f32_32x32x64_f8f6f4 v[114:129], v[210:217], v[146:153], v[114:129]
	v_add_f32_e32 v209, v103, v209
	v_exp_f32_e32 v108, v108
	v_exp_f32_e32 v110, v110
	v_exp_f32_e32 v111, v111
	v_add_f32_e32 v209, v104, v209
	v_exp_f32_e32 v109, v109
	v_add_f32_e32 v209, v105, v209
	v_add_f32_e32 v209, v106, v209
	v_add_f32_e32 v209, v107, v209
	v_exp_f32_e32 v112, v112
	v_exp_f32_e32 v113, v113
	v_add_f32_e32 v209, v108, v209
	v_cvt_pk_fp8_f32 v130, v182, v183
	v_cvt_pk_fp8_f32 v134, v98, v99
	v_cvt_pk_fp8_f32 v131, v226, v227
	v_mfma_f32_32x32x64_f8f6f4 v[82:97], v[218:225], v[146:153], v[82:97]
	ds_read_b128 v[210:213], v200 offset:49152
	ds_read_b128 v[214:217], v201 offset:49152
	ds_read_b128 v[218:221], v200 offset:55296
	ds_read_b128 v[222:225], v201 offset:55296
	v_cvt_pk_fp8_f32 v135, v102, v103
	v_cvt_pk_fp8_f32 v132, v230, v231
	v_cvt_pk_fp8_f32 v136, v106, v107
	v_cvt_pk_fp8_f32 v133, v234, v235
	v_cvt_pk_fp8_f32 v137, v110, v111
	v_add_f32_e32 v209, v109, v209
	v_add_f32_e32 v209, v110, v209
	v_add_f32_e32 v209, v111, v209
	v_add_f32_e32 v209, v112, v209
	v_cvt_pk_fp8_f32 v130, v184, v185 op_sel:[0,0,1]
	v_cvt_pk_fp8_f32 v134, v100, v101 op_sel:[0,0,1]
	v_cvt_pk_fp8_f32 v131, v228, v229 op_sel:[0,0,1]
	v_cvt_pk_fp8_f32 v135, v104, v105 op_sel:[0,0,1]
	v_cvt_pk_fp8_f32 v132, v232, v233 op_sel:[0,0,1]
	s_waitcnt lgkmcnt(0)
	v_mfma_f32_32x32x64_f8f6f4 v[114:129], v[210:217], v[154:161], v[114:129]
	v_cvt_pk_fp8_f32 v136, v108, v109 op_sel:[0,0,1]
	v_cvt_pk_fp8_f32 v133, v236, v237 op_sel:[0,0,1]
	v_cvt_pk_fp8_f32 v137, v112, v113 op_sel:[0,0,1]
	v_add_f32_e32 v209, v113, v209
	v_mov_b32_e32 v210, v209
	s_nop 1
	v_permlane32_swap_b32_e32 v209, v210
	v_mfma_f32_32x32x64_f8f6f4 v[82:97], v[218:225], v[154:161], v[82:97]
	s_cmp_eq_u32 s94, 0
	s_cbranch_scc0 .Lstg_mid1_l0
	s_waitcnt vmcnt(0)
	s_barrier
	s_mov_b32 m0, s92
	s_nop 0
	global_load_lds_dwordx4 v164, s[24:25]
	s_mov_b32 m0, s86
	s_nop 0
	global_load_lds_dwordx4 v170, s[26:27]
	s_add_u32 s24, s24, 0x3000
	s_addc_u32 s25, s25, 0
	s_add_u32 s26, s26, 64
	s_addc_u32 s27, s27, 0
.Lstg_mid1_l0:
	ds_read_b128 v[102:105], v194 offset:32768
	ds_read_b128 v[98:101], v193 offset:32768
	ds_read_b128 v[106:109], v193 offset:34816
	ds_read_b128 v[110:113], v194 offset:34816
	s_nop 6
	v_max_f32_e32 v182, v114, v115
	v_max_f32_e32 v183, v114, v114
	s_waitcnt lgkmcnt(0)
	v_mfma_f32_32x32x64_f8f6f4 v[2:17], v[130:137], v[98:105], v[2:17]
	v_max3_f32 v182, v182, v116, v117
	v_max3_f32 v182, v182, v118, v119
	v_max3_f32 v182, v182, v120, v121
	v_max3_f32 v182, v182, v122, v123
	v_max3_f32 v182, v182, v124, v125
	v_max3_f32 v182, v182, v126, v127
	v_max3_f32 v182, v182, v128, v129
	v_max3_f32 v182, v182, v82, v83
	v_mov_b32_e32 v211, 1.0
	v_mfma_f32_32x32x64_f8f6f4 v[50:65], v[130:137], v[106:113], v[50:65]
	ds_read_b128 v[98:101], v193 offset:36864
	ds_read_b128 v[106:109], v193 offset:38912
	ds_read_b128 v[102:105], v194 offset:36864
	ds_read_b128 v[110:113], v194 offset:38912
	s_waitcnt lgkmcnt(0)
	v_mfma_f32_32x32x64_f8f6f4 v[34:49], v[130:137], v[98:105], v[34:49]
	v_max3_f32 v98, v182, v84, v85
	v_max3_f32 v98, v98, v86, v87
	v_max3_f32 v98, v98, v88, v89
	v_max3_f32 v98, v98, v90, v91
	v_max3_f32 v98, v98, v92, v93
	v_max3_f32 v98, v98, v94, v95
	v_max3_f32 v98, v98, v96, v97
	v_mov_b32_e32 v99, v98
	s_nop 1
	v_permlane32_swap_b32_e32 v98, v99
	v_max_f32_e32 v98, v98, v99
	v_cmp_ge_f32_e32 vcc, s85, v98
	s_cmp_eq_u64 vcc, exec
	v_mfma_f32_32x32x64_f8f6f4 v[18:33], v[130:137], v[106:113], v[18:33]
	s_cbranch_scc0 .LBB0_932
	s_setprio 0
	s_branch .LBB0_901

; template <bool FIRST>
; __device__ __forceinline__ void partialSM(f32x16& p0, f32x16& p1, float& m_reg, f32x16& nm16, float& alpha) {
;   float pmax = p0[0];
; #pragma unroll
;   for (int r = 1; r < 16; ++r) pmax = fmaxf(pmax, p0[r]);
; #pragma unroll
;   for (int r = 0; r < 16; ++r) pmax = fmaxf(pmax, p1[r]);
;   { auto rr = __builtin_amdgcn_permlane32_swap(__float_as_uint(pmax), __float_as_uint(pmax), false, false);
;     pmax = fmaxf(__uint_as_float(rr[0]), __uint_as_float(rr[1])); }
;   if (!FIRST && __builtin_expect(__all(pmax <= THR2), 1)) { alpha = 1.f; }
;   else { const float d = FIRST ? pmax : fmaxf(pmax, 0.f);
;     alpha = FIRST ? 1.f : __builtin_amdgcn_exp2f(-d); m_reg += d;
;     const float nm = -m_reg;
; #pragma unroll
;     for (int r = 0; r < 16; ++r) { p0[r] -= d; p1[r] -= d; float t = nm16[r]; asm volatile("v_mov_b32 %0, %1" : "+v"(t) : "v"(nm)); nm16[r] = t; } }
; #pragma unroll
;   for (int r = 0; r < 16; ++r) p0[r] = __builtin_amdgcn_exp2f(p0[r]);
; }
; __device__ __forceinline__ void finishSM(f32x16& p0, f32x16& p1, float alpha, float& l_reg, v8i& pa) {
; #pragma unroll
;   for (int r = 0; r < 16; ++r) p1[r] = __builtin_amdgcn_exp2f(p1[r]);
;   float ps = 0;
; #pragma unroll
;   for (int r = 0; r < 16; ++r) ps += p0[r];
; #pragma unroll
;   for (int r = 0; r < 16; ++r) ps += p1[r];
;   { auto rr = __builtin_amdgcn_permlane32_swap(__float_as_uint(ps), __float_as_uint(ps), false, false);
;     ps = __uint_as_float(rr[0]) + __uint_as_float(rr[1]); }
;   l_reg = l_reg * alpha + ps;
; #pragma unroll
;   for (int q = 0; q < 4; ++q) { int w0 = pa[q], w1 = pa[4 + q];
;     w0 = __builtin_amdgcn_cvt_pk_fp8_f32(p0[4 * q], p0[4 * q + 1], w0, false); w0 = __builtin_amdgcn_cvt_pk_fp8_f32(p0[4 * q + 2], p0[4 * q + 3], w0, true);
;     w1 = __builtin_amdgcn_cvt_pk_fp8_f32(p1[4 * q], p1[4 * q + 1], w1, false); w1 = __builtin_amdgcn_cvt_pk_fp8_f32(p1[4 * q + 2], p1[4 * q + 3], w1, true);
;     pa[q] = w0; pa[4 + q] = w1; }
; }
; __device__ __forceinline__ void qkt(f32x16& p0, f32x16& p1, const char* Ks, const v8i* qr, int r32, int hi, const f32x16& nm16) {
; #pragma unroll
;   for (int s = 0; s < 3; ++s) { const int c0 = 4 * s + 2 * hi;
;     const v8i a0 = __builtin_shufflevector(*reinterpret_cast<const v4i*>(Ks + k8_off(r32, c0)), *reinterpret_cast<const v4i*>(Ks + k8_off(r32, c0 + 1)), 0, 1, 2, 3, 4, 5, 6, 7);
.Lstg_end1_l0:
	v_exp_f32_e32 v182, v114
	v_exp_f32_e32 v183, v115
	v_exp_f32_e32 v184, v116
	v_exp_f32_e32 v185, v117
	v_exp_f32_e32 v228, v118
	v_exp_f32_e32 v229, v119
	v_exp_f32_e32 v230, v120
	v_exp_f32_e32 v231, v121
	v_exp_f32_e32 v232, v122
	v_exp_f32_e32 v233, v123
	v_exp_f32_e32 v234, v124
	v_exp_f32_e32 v235, v125
	v_exp_f32_e32 v236, v126
	v_exp_f32_e32 v237, v127
	v_exp_f32_e32 v238, v128
	v_exp_f32_e32 v239, v129
	ds_read_b128 v[98:101], v196 offset:8192
	ds_read_b128 v[102:105], v197 offset:8192
	ds_read_b128 v[212:215], v196 offset:14336
	ds_read_b128 v[216:219], v197 offset:14336
	v_exp_f32_e32 v82, v82
	v_exp_f32_e32 v83, v83
	s_waitcnt lgkmcnt(0)
	v_mfma_f32_32x32x64_f8f6f4 v[114:129], v[98:105], v[138:145], v[66:81]
	v_exp_f32_e32 v84, v84
	v_exp_f32_e32 v85, v85
	v_exp_f32_e32 v86, v86
	v_exp_f32_e32 v87, v87
	v_exp_f32_e32 v88, v88
	v_exp_f32_e32 v89, v89
	v_exp_f32_e32 v90, v90
	v_exp_f32_e32 v91, v91
	v_exp_f32_e32 v92, v92
	v_exp_f32_e32 v94, v94
	v_exp_f32_e32 v95, v95
	v_exp_f32_e32 v93, v93
	v_exp_f32_e32 v96, v96
	v_exp_f32_e32 v97, v97
	v_cvt_pk_fp8_f32 v130, v182, v183
	v_mfma_f32_32x32x64_f8f6f4 v[98:113], v[212:219], v[138:145], v[66:81]
	ds_read_b128 v[212:215], v198 offset:8192
	ds_read_b128 v[216:219], v199 offset:8192
	ds_read_b128 v[220:223], v198 offset:14336
	ds_read_b128 v[224:227], v199 offset:14336
	s_setprio 1
	v_cvt_pk_fp8_f32 v134, v82, v83
	v_cvt_pk_fp8_f32 v131, v228, v229
	v_cvt_pk_fp8_f32 v135, v86, v87
	v_cvt_pk_fp8_f32 v132, v232, v233
	v_cvt_pk_fp8_f32 v136, v90, v91
	v_cvt_pk_fp8_f32 v133, v236, v237
	v_cvt_pk_fp8_f32 v137, v94, v95
	v_cvt_pk_fp8_f32 v130, v184, v185 op_sel:[0,0,1]
	v_cvt_pk_fp8_f32 v134, v84, v85 op_sel:[0,0,1]
	v_cvt_pk_fp8_f32 v131, v230, v231 op_sel:[0,0,1]
	v_cvt_pk_fp8_f32 v135, v88, v89 op_sel:[0,0,1]
	v_cvt_pk_fp8_f32 v132, v234, v235 op_sel:[0,0,1]
	v_cvt_pk_fp8_f32 v136, v92, v93 op_sel:[0,0,1]
	v_cvt_pk_fp8_f32 v133, v238, v239 op_sel:[0,0,1]
	s_waitcnt lgkmcnt(0)
	v_mfma_f32_32x32x64_f8f6f4 v[114:129], v[212:219], v[146:153], v[114:129]
	v_cvt_pk_fp8_f32 v137, v96, v97 op_sel:[0,0,1]
	v_mfma_f32_32x32x64_f8f6f4 v[98:113], v[220:227], v[146:153], v[98:113]
	ds_read_b128 v[212:215], v200 offset:8192
	ds_read_b128 v[216:219], v201 offset:8192
	ds_read_b128 v[220:223], v200 offset:14336
	ds_read_b128 v[224:227], v201 offset:14336
	s_waitcnt lgkmcnt(0)
	v_mfma_f32_32x32x64_f8f6f4 v[114:129], v[212:219], v[154:161], v[114:129]
	v_add_f32_e32 v212, 0, v182
	v_add_f32_e32 v212, v183, v212
	v_add_f32_e32 v212, v184, v212
	v_add_f32_e32 v212, v185, v212
	v_add_f32_e32 v212, v228, v212
	v_add_f32_e32 v212, v229, v212
	v_add_f32_e32 v212, v230, v212
	v_add_f32_e32 v212, v231, v212
	v_add_f32_e32 v212, v232, v212
	v_add_f32_e32 v212, v233, v212
	v_add_f32_e32 v212, v234, v212
	v_add_f32_e32 v212, v235, v212
	v_add_f32_e32 v212, v236, v212
	v_add_f32_e32 v212, v237, v212
	v_add_f32_e32 v212, v238, v212
	v_add_f32_e32 v212, v239, v212
	v_add_f32_e32 v212, v82, v212
	v_add_f32_e32 v212, v83, v212
	v_mfma_f32_32x32x64_f8f6f4 v[98:113], v[220:227], v[154:161], v[98:113]
	v_add_f32_e32 v212, v84, v212
	v_add_f32_e32 v212, v85, v212
	v_add_f32_e32 v212, v86, v212
	v_add_f32_e32 v212, v87, v212
	v_add_f32_e32 v212, v88, v212
	v_add_f32_e32 v212, v89, v212
	v_add_f32_e32 v212, v90, v212
	v_add_f32_e32 v212, v91, v212
	v_add_f32_e32 v212, v92, v212
	v_add_f32_e32 v212, v93, v212
	v_add_f32_e32 v212, v94, v212
	v_add_f32_e32 v212, v95, v212
	v_add_f32_e32 v212, v96, v212
	v_add_f32_e32 v212, v97, v212
	v_mov_b32_e32 v213, v212
	s_nop 1
	v_permlane32_swap_b32_e32 v212, v213
	s_cmp_eq_u32 s94, 0
	s_cbranch_scc0 .Lstg_mid2_l0
	s_waitcnt vmcnt(0)
	s_barrier
	s_mov_b32 m0, s90
	s_nop 0
	global_load_lds_dwordx4 v164, s[24:25]
	s_mov_b32 m0, s88
	s_nop 0
	global_load_lds_dwordx4 v170, s[26:27]
	s_add_u32 s24, s24, 0x3000
	s_addc_u32 s25, s25, 0
	s_add_u32 s26, s26, 64
	s_addc_u32 s27, s27, 0
.Lstg_mid2_l0:
	ds_read_b128 v[86:89], v194 offset:40960
	ds_read_b128 v[82:85], v193 offset:40960
	ds_read_b128 v[90:93], v193 offset:43008
	ds_read_b128 v[94:97], v194 offset:43008
	v_max_f32_e32 v182, v114, v115
	v_max_f32_e32 v183, v114, v114
	s_waitcnt lgkmcnt(0)
	v_mfma_f32_32x32x64_f8f6f4 v[2:17], v[130:137], v[82:89], v[2:17]
	v_max3_f32 v182, v182, v116, v117
	v_max3_f32 v182, v182, v118, v119
	v_max3_f32 v182, v182, v120, v121
	v_max3_f32 v182, v182, v122, v123
	v_max3_f32 v182, v182, v124, v125
	v_max3_f32 v182, v182, v126, v127
	v_max3_f32 v182, v182, v128, v129
	v_max3_f32 v182, v182, v98, v99
	v_mov_b32_e32 v214, 1.0
	v_mfma_f32_32x32x64_f8f6f4 v[50:65], v[130:137], v[90:97], v[50:65]
	ds_read_b128 v[82:85], v193 offset:45056
	ds_read_b128 v[90:93], v193 offset:47104
	ds_read_b128 v[86:89], v194 offset:45056
	ds_read_b128 v[94:97], v194 offset:47104
	s_waitcnt lgkmcnt(0)
	v_mfma_f32_32x32x64_f8f6f4 v[34:49], v[130:137], v[82:89], v[34:49]
	v_max3_f32 v82, v182, v100, v101
	v_max3_f32 v82, v82, v102, v103
	v_max3_f32 v82, v82, v104, v105
	v_max3_f32 v82, v82, v106, v107
	v_max3_f32 v82, v82, v108, v109
	v_max3_f32 v82, v82, v110, v111
	v_max3_f32 v82, v82, v112, v113
	v_mov_b32_e32 v83, v82
	s_nop 1
	v_permlane32_swap_b32_e32 v82, v83
	v_max_f32_e32 v82, v82, v83
	v_cmp_ge_f32_e32 vcc, s85, v82
	s_cmp_eq_u64 vcc, exec
	v_mfma_f32_32x32x64_f8f6f4 v[18:33], v[130:137], v[90:97], v[18:33]
	s_cbranch_scc0 .LBB0_933
	s_setprio 0
	s_branch .LBB0_908

; template <bool FIRST>
; __device__ __forceinline__ void partialSM(f32x16& p0, f32x16& p1, float& m_reg, f32x16& nm16, float& alpha) {
;   float pmax = p0[0];
; #pragma unroll
;   for (int r = 1; r < 16; ++r) pmax = fmaxf(pmax, p0[r]);
; #pragma unroll
;   for (int r = 0; r < 16; ++r) pmax = fmaxf(pmax, p1[r]);
;   { auto rr = __builtin_amdgcn_permlane32_swap(__float_as_uint(pmax), __float_as_uint(pmax), false, false);
;     pmax = fmaxf(__uint_as_float(rr[0]), __uint_as_float(rr[1])); }
;   if (!FIRST && __builtin_expect(__all(pmax <= THR2), 1)) { alpha = 1.f; }
;   else { const float d = FIRST ? pmax : fmaxf(pmax, 0.f);
;     alpha = FIRST ? 1.f : __builtin_amdgcn_exp2f(-d); m_reg += d;
;     const float nm = -m_reg;
; #pragma unroll
;     for (int r = 0; r < 16; ++r) { p0[r] -= d; p1[r] -= d; float t = nm16[r]; asm volatile("v_mov_b32 %0, %1" : "+v"(t) : "v"(nm)); nm16[r] = t; } }
; #pragma unroll
;   for (int r = 0; r < 16; ++r) p0[r] = __builtin_amdgcn_exp2f(p0[r]);
; }
; __device__ __forceinline__ void finishSM(f32x16& p0, f32x16& p1, float alpha, float& l_reg, v8i& pa) {
; #pragma unroll
;   for (int r = 0; r < 16; ++r) p1[r] = __builtin_amdgcn_exp2f(p1[r]);
;   float ps = 0;
; #pragma unroll
;   for (int r = 0; r < 16; ++r) ps += p0[r];
; #pragma unroll
;   for (int r = 0; r < 16; ++r) ps += p1[r];
;   { auto rr = __builtin_amdgcn_permlane32_swap(__float_as_uint(ps), __float_as_uint(ps), false, false);
;     ps = __uint_as_float(rr[0]) + __uint_as_float(rr[1]); }
;   l_reg = l_reg * alpha + ps;
; #pragma unroll
;   for (int q = 0; q < 4; ++q) { int w0 = pa[q], w1 = pa[4 + q];
;     w0 = __builtin_amdgcn_cvt_pk_fp8_f32(p0[4 * q], p0[4 * q + 1], w0, false); w0 = __builtin_amdgcn_cvt_pk_fp8_f32(p0[4 * q + 2], p0[4 * q + 3], w0, true);
;     w1 = __builtin_amdgcn_cvt_pk_fp8_f32(p1[4 * q], p1[4 * q + 1], w1, false); w1 = __builtin_amdgcn_cvt_pk_fp8_f32(p1[4 * q + 2], p1[4 * q + 3], w1, true);
;     pa[q] = w0; pa[4 + q] = w1; }
; }
; __device__ __forceinline__ void qkt(f32x16& p0, f32x16& p1, const char* Ks, const v8i* qr, int r32, int hi, const f32x16& nm16) {
; #pragma unroll
;   for (int s = 0; s < 3; ++s) { const int c0 = 4 * s + 2 * hi;
;     const v8i a0 = __builtin_shufflevector(*reinterpret_cast<const v4i*>(Ks + k8_off(r32, c0)), *reinterpret_cast<const v4i*>(Ks + k8_off(r32, c0 + 1)), 0, 1, 2, 3, 4, 5, 6, 7);
.Lstg_end2_l0:
	v_exp_f32_e32 v182, v114
	v_exp_f32_e32 v183, v115
	v_exp_f32_e32 v184, v116
	v_exp_f32_e32 v185, v117
	v_exp_f32_e32 v232, v118
	v_exp_f32_e32 v233, v119
	v_exp_f32_e32 v234, v120
	v_exp_f32_e32 v235, v121
	v_exp_f32_e32 v236, v122
	v_exp_f32_e32 v237, v123
	v_exp_f32_e32 v238, v124
	v_exp_f32_e32 v239, v125
	v_exp_f32_e32 v240, v126
	v_exp_f32_e32 v241, v127
	v_exp_f32_e32 v242, v128
	v_exp_f32_e32 v243, v129
	ds_read_b128 v[82:85], v196 offset:20480
	ds_read_b128 v[86:89], v197 offset:20480
	ds_read_b128 v[216:219], v196 offset:26624
	ds_read_b128 v[220:223], v197 offset:26624
	v_add_f32_e32 v215, 0, v182
	v_add_f32_e32 v215, v183, v215
	s_waitcnt lgkmcnt(0)
	v_mfma_f32_32x32x64_f8f6f4 v[114:129], v[82:89], v[138:145], v[66:81]
	v_add_f32_e32 v215, v184, v215
	v_add_f32_e32 v215, v185, v215
	v_add_f32_e32 v215, v232, v215
	v_add_f32_e32 v215, v233, v215
	v_add_f32_e32 v215, v234, v215
	v_add_f32_e32 v215, v235, v215
	v_add_f32_e32 v215, v236, v215
	v_add_f32_e32 v215, v237, v215
	v_add_f32_e32 v215, v238, v215
	v_add_f32_e32 v215, v239, v215
	v_exp_f32_e32 v98, v98
	v_add_f32_e32 v215, v240, v215
	v_exp_f32_e32 v99, v99
	v_add_f32_e32 v215, v241, v215
	v_exp_f32_e32 v100, v100
	v_mfma_f32_32x32x64_f8f6f4 v[82:97], v[216:223], v[138:145], v[66:81]
	ds_read_b128 v[216:219], v198 offset:20480
	ds_read_b128 v[220:223], v199 offset:20480
	ds_read_b128 v[224:227], v198 offset:26624
	ds_read_b128 v[228:231], v199 offset:26624
	s_setprio 1
	v_add_f32_e32 v215, v242, v215
	v_exp_f32_e32 v101, v101
	v_add_f32_e32 v215, v243, v215
	v_exp_f32_e32 v102, v102
	v_add_f32_e32 v215, v98, v215
	v_exp_f32_e32 v103, v103
	v_add_f32_e32 v215, v99, v215
	v_exp_f32_e32 v104, v104
	v_add_f32_e32 v215, v100, v215
	v_exp_f32_e32 v105, v105
	v_add_f32_e32 v215, v101, v215
	v_exp_f32_e32 v106, v106
	v_add_f32_e32 v215, v102, v215
	v_exp_f32_e32 v107, v107
	s_waitcnt lgkmcnt(0)
	v_mfma_f32_32x32x64_f8f6f4 v[114:129], v[216:223], v[146:153], v[114:129]
	v_add_f32_e32 v215, v103, v215
	v_exp_f32_e32 v108, v108
	v_exp_f32_e32 v110, v110
	v_exp_f32_e32 v111, v111
	v_add_f32_e32 v215, v104, v215
	v_exp_f32_e32 v109, v109
	v_add_f32_e32 v215, v105, v215
	v_add_f32_e32 v215, v106, v215
	v_add_f32_e32 v215, v107, v215
	v_exp_f32_e32 v112, v112
	v_exp_f32_e32 v113, v113
	v_add_f32_e32 v215, v108, v215
	v_cvt_pk_fp8_f32 v130, v182, v183
	v_cvt_pk_fp8_f32 v134, v98, v99
	v_cvt_pk_fp8_f32 v131, v232, v233
	v_mfma_f32_32x32x64_f8f6f4 v[82:97], v[224:231], v[146:153], v[82:97]
	ds_read_b128 v[216:219], v200 offset:20480
	ds_read_b128 v[220:223], v201 offset:20480
	ds_read_b128 v[224:227], v200 offset:26624
	ds_read_b128 v[228:231], v201 offset:26624
	v_cvt_pk_fp8_f32 v135, v102, v103
	v_cvt_pk_fp8_f32 v132, v236, v237
	v_cvt_pk_fp8_f32 v136, v106, v107
	v_cvt_pk_fp8_f32 v133, v240, v241
	v_cvt_pk_fp8_f32 v137, v110, v111
	v_add_f32_e32 v215, v109, v215
	v_add_f32_e32 v215, v110, v215
	v_add_f32_e32 v215, v111, v215
	v_add_f32_e32 v215, v112, v215
	v_cvt_pk_fp8_f32 v130, v184, v185 op_sel:[0,0,1]
	v_cvt_pk_fp8_f32 v134, v100, v101 op_sel:[0,0,1]
	v_cvt_pk_fp8_f32 v131, v234, v235 op_sel:[0,0,1]
	v_cvt_pk_fp8_f32 v135, v104, v105 op_sel:[0,0,1]
	v_cvt_pk_fp8_f32 v132, v238, v239 op_sel:[0,0,1]
	s_waitcnt lgkmcnt(0)
	v_mfma_f32_32x32x64_f8f6f4 v[114:129], v[216:223], v[154:161], v[114:129]
	v_cvt_pk_fp8_f32 v136, v108, v109 op_sel:[0,0,1]
	v_cvt_pk_fp8_f32 v133, v242, v243 op_sel:[0,0,1]
	v_cvt_pk_fp8_f32 v137, v112, v113 op_sel:[0,0,1]
	v_add_f32_e32 v215, v113, v215
	v_mov_b32_e32 v216, v215
	s_nop 1
	v_permlane32_swap_b32_e32 v215, v216
	v_mfma_f32_32x32x64_f8f6f4 v[82:97], v[224:231], v[154:161], v[82:97]
	s_cmp_eq_u32 s94, 0
	s_cbranch_scc0 .Lstg_mid3_l0
	s_waitcnt vmcnt(0)
	s_barrier
	s_mov_b32 m0, s87
	s_nop 0
	global_load_lds_dwordx4 v164, s[24:25]
	s_mov_b32 m0, s89
	s_nop 0
	global_load_lds_dwordx4 v170, s[26:27]
	s_add_u32 s24, s24, 0x3000
	s_addc_u32 s25, s25, 0
	s_add_u32 s26, s26, 64
	s_addc_u32 s27, s27, 0
.Lstg_mid3_l0:
	ds_read_b128 v[102:105], v194
	ds_read_b128 v[98:101], v193
	ds_read_b128 v[106:109], v193 offset:2048
	ds_read_b128 v[110:113], v194 offset:2048
	s_nop 6
	v_max_f32_e32 v182, v114, v115
	v_max_f32_e32 v183, v114, v114
	s_waitcnt lgkmcnt(0)
	v_mfma_f32_32x32x64_f8f6f4 v[2:17], v[130:137], v[98:105], v[2:17]
	v_max3_f32 v182, v182, v116, v117
	v_max3_f32 v182, v182, v118, v119
	v_max3_f32 v182, v182, v120, v121
	v_max3_f32 v182, v182, v122, v123
	v_max3_f32 v182, v182, v124, v125
	v_max3_f32 v182, v182, v126, v127
	v_max3_f32 v182, v182, v128, v129
	v_max3_f32 v182, v182, v82, v83
	v_mov_b32_e32 v217, 1.0
	v_mfma_f32_32x32x64_f8f6f4 v[50:65], v[130:137], v[106:113], v[50:65]
	ds_read_b128 v[98:101], v193 offset:4096
	ds_read_b128 v[106:109], v193 offset:6144
	ds_read_b128 v[102:105], v194 offset:4096
	ds_read_b128 v[110:113], v194 offset:6144
	s_waitcnt lgkmcnt(0)
	v_mfma_f32_32x32x64_f8f6f4 v[34:49], v[130:137], v[98:105], v[34:49]
	v_max3_f32 v98, v182, v84, v85
	v_max3_f32 v98, v98, v86, v87
	v_max3_f32 v98, v98, v88, v89
	v_max3_f32 v98, v98, v90, v91
	v_max3_f32 v98, v98, v92, v93
	v_max3_f32 v98, v98, v94, v95
	v_max3_f32 v98, v98, v96, v97
	v_mov_b32_e32 v99, v98
	s_nop 1
	v_permlane32_swap_b32_e32 v98, v99
	v_max_f32_e32 v98, v98, v99
	v_cmp_ge_f32_e32 vcc, s85, v98
	s_cmp_eq_u64 vcc, exec
	v_mfma_f32_32x32x64_f8f6f4 v[18:33], v[130:137], v[106:113], v[18:33]
	s_cbranch_scc0 .LBB0_934
	s_setprio 0
	s_branch .LBB0_915

; template <bool FIRST>
; __device__ __forceinline__ void partialSM(f32x16& p0, f32x16& p1, float& m_reg, f32x16& nm16, float& alpha) {
;   float pmax = p0[0];
; #pragma unroll
;   for (int r = 1; r < 16; ++r) pmax = fmaxf(pmax, p0[r]);
; #pragma unroll
;   for (int r = 0; r < 16; ++r) pmax = fmaxf(pmax, p1[r]);
;   { auto rr = __builtin_amdgcn_permlane32_swap(__float_as_uint(pmax), __float_as_uint(pmax), false, false);
;     pmax = fmaxf(__uint_as_float(rr[0]), __uint_as_float(rr[1])); }
;   if (!FIRST && __builtin_expect(__all(pmax <= THR2), 1)) { alpha = 1.f; }
;   else { const float d = FIRST ? pmax : fmaxf(pmax, 0.f);
;     alpha = FIRST ? 1.f : __builtin_amdgcn_exp2f(-d); m_reg += d;
;     const float nm = -m_reg;
; #pragma unroll
;     for (int r = 0; r < 16; ++r) { p0[r] -= d; p1[r] -= d; float t = nm16[r]; asm volatile("v_mov_b32 %0, %1" : "+v"(t) : "v"(nm)); nm16[r] = t; } }
; #pragma unroll
;   for (int r = 0; r < 16; ++r) p0[r] = __builtin_amdgcn_exp2f(p0[r]);
; }
; __device__ __forceinline__ void finishSM(f32x16& p0, f32x16& p1, float alpha, float& l_reg, v8i& pa) {
; #pragma unroll
;   for (int r = 0; r < 16; ++r) p1[r] = __builtin_amdgcn_exp2f(p1[r]);
;   float ps = 0;
; #pragma unroll
;   for (int r = 0; r < 16; ++r) ps += p0[r];
; #pragma unroll
;   for (int r = 0; r < 16; ++r) ps += p1[r];
;   { auto rr = __builtin_amdgcn_permlane32_swap(__float_as_uint(ps), __float_as_uint(ps), false, false);
;     ps = __uint_as_float(rr[0]) + __uint_as_float(rr[1]); }
;   l_reg = l_reg * alpha + ps;
; #pragma unroll
;   for (int q = 0; q < 4; ++q) { int w0 = pa[q], w1 = pa[4 + q];
;     w0 = __builtin_amdgcn_cvt_pk_fp8_f32(p0[4 * q], p0[4 * q + 1], w0, false); w0 = __builtin_amdgcn_cvt_pk_fp8_f32(p0[4 * q + 2], p0[4 * q + 3], w0, true);
;     w1 = __builtin_amdgcn_cvt_pk_fp8_f32(p1[4 * q], p1[4 * q + 1], w1, false); w1 = __builtin_amdgcn_cvt_pk_fp8_f32(p1[4 * q + 2], p1[4 * q + 3], w1, true);
;     pa[q] = w0; pa[4 + q] = w1; }
; }
; __device__ __forceinline__ void qkt(f32x16& p0, f32x16& p1, const char* Ks, const v8i* qr, int r32, int hi, const f32x16& nm16) {
; #pragma unroll
;   for (int s = 0; s < 3; ++s) { const int c0 = 4 * s + 2 * hi;
;     const v8i a0 = __builtin_shufflevector(*reinterpret_cast<const v4i*>(Ks + k8_off(r32, c0)), *reinterpret_cast<const v4i*>(Ks + k8_off(r32, c0 + 1)), 0, 1, 2, 3, 4, 5, 6, 7);
.Lstg_end3_l0:
	v_exp_f32_e32 v182, v114
	v_exp_f32_e32 v183, v115
	v_exp_f32_e32 v184, v116
	v_exp_f32_e32 v185, v117
	v_exp_f32_e32 v234, v118
	v_exp_f32_e32 v235, v119
	v_exp_f32_e32 v236, v120
	v_exp_f32_e32 v237, v121
	v_exp_f32_e32 v238, v122
	v_exp_f32_e32 v239, v123
	v_exp_f32_e32 v240, v124
	v_exp_f32_e32 v241, v125
	v_exp_f32_e32 v242, v126
	v_exp_f32_e32 v243, v127
	v_exp_f32_e32 v244, v128
	v_exp_f32_e32 v245, v129
	ds_read_b128 v[98:101], v196 offset:49152
	ds_read_b128 v[102:105], v197 offset:49152
	ds_read_b128 v[218:221], v196 offset:55296
	ds_read_b128 v[222:225], v197 offset:55296
	v_exp_f32_e32 v82, v82
	v_exp_f32_e32 v83, v83
	s_waitcnt lgkmcnt(0)
	v_mfma_f32_32x32x64_f8f6f4 v[114:129], v[98:105], v[138:145], v[66:81]
	v_exp_f32_e32 v84, v84
	v_exp_f32_e32 v85, v85
	v_exp_f32_e32 v86, v86
	v_exp_f32_e32 v87, v87
	v_exp_f32_e32 v88, v88
	v_exp_f32_e32 v89, v89
	v_exp_f32_e32 v90, v90
	v_exp_f32_e32 v91, v91
	v_exp_f32_e32 v92, v92
	v_exp_f32_e32 v94, v94
	v_exp_f32_e32 v95, v95
	v_exp_f32_e32 v93, v93
	v_exp_f32_e32 v96, v96
	v_exp_f32_e32 v97, v97
	v_cvt_pk_fp8_f32 v130, v182, v183
	v_mfma_f32_32x32x64_f8f6f4 v[98:113], v[218:225], v[138:145], v[66:81]
	ds_read_b128 v[218:221], v198 offset:49152
	ds_read_b128 v[222:225], v199 offset:49152
	ds_read_b128 v[226:229], v198 offset:55296
	ds_read_b128 v[230:233], v199 offset:55296
	s_setprio 1
	v_cvt_pk_fp8_f32 v134, v82, v83
	v_cvt_pk_fp8_f32 v131, v234, v235
	v_cvt_pk_fp8_f32 v135, v86, v87
	v_cvt_pk_fp8_f32 v132, v238, v239
	v_cvt_pk_fp8_f32 v136, v90, v91
	v_cvt_pk_fp8_f32 v133, v242, v243
	v_cvt_pk_fp8_f32 v137, v94, v95
	v_cvt_pk_fp8_f32 v130, v184, v185 op_sel:[0,0,1]
	v_cvt_pk_fp8_f32 v134, v84, v85 op_sel:[0,0,1]
	v_cvt_pk_fp8_f32 v131, v236, v237 op_sel:[0,0,1]
	v_cvt_pk_fp8_f32 v135, v88, v89 op_sel:[0,0,1]
	v_cvt_pk_fp8_f32 v132, v240, v241 op_sel:[0,0,1]
	v_cvt_pk_fp8_f32 v136, v92, v93 op_sel:[0,0,1]
	v_cvt_pk_fp8_f32 v133, v244, v245 op_sel:[0,0,1]
	s_waitcnt lgkmcnt(0)
	v_mfma_f32_32x32x64_f8f6f4 v[114:129], v[218:225], v[146:153], v[114:129]
	v_cvt_pk_fp8_f32 v137, v96, v97 op_sel:[0,0,1]
	v_mfma_f32_32x32x64_f8f6f4 v[98:113], v[226:233], v[146:153], v[98:113]
	ds_read_b128 v[218:221], v200 offset:49152
	ds_read_b128 v[222:225], v201 offset:49152
	ds_read_b128 v[226:229], v200 offset:55296
	ds_read_b128 v[230:233], v201 offset:55296
	s_waitcnt lgkmcnt(0)
	v_mfma_f32_32x32x64_f8f6f4 v[114:129], v[218:225], v[154:161], v[114:129]
	v_add_f32_e32 v218, 0, v182
	v_add_f32_e32 v218, v183, v218
	v_add_f32_e32 v218, v184, v218
	v_add_f32_e32 v218, v185, v218
	v_add_f32_e32 v218, v234, v218
	v_add_f32_e32 v218, v235, v218
	v_add_f32_e32 v218, v236, v218
	v_add_f32_e32 v218, v237, v218
	v_add_f32_e32 v218, v238, v218
	v_add_f32_e32 v218, v239, v218
	v_add_f32_e32 v218, v240, v218
	v_add_f32_e32 v218, v241, v218
	v_add_f32_e32 v218, v242, v218
	v_add_f32_e32 v218, v243, v218
	v_add_f32_e32 v218, v244, v218
	v_add_f32_e32 v218, v245, v218
	v_add_f32_e32 v218, v82, v218
	v_add_f32_e32 v218, v83, v218
	v_mfma_f32_32x32x64_f8f6f4 v[98:113], v[226:233], v[154:161], v[98:113]
	v_add_f32_e32 v218, v84, v218
	v_add_f32_e32 v218, v85, v218
	v_add_f32_e32 v218, v86, v218
	v_add_f32_e32 v218, v87, v218
	v_add_f32_e32 v218, v88, v218
	v_add_f32_e32 v218, v89, v218
	v_add_f32_e32 v218, v90, v218
	v_add_f32_e32 v218, v91, v218
	v_add_f32_e32 v218, v92, v218
	v_add_f32_e32 v218, v93, v218
	v_add_f32_e32 v218, v94, v218
	v_add_f32_e32 v218, v95, v218
	v_add_f32_e32 v218, v96, v218
	v_add_f32_e32 v218, v97, v218
	v_mov_b32_e32 v219, v218
	s_nop 1
	v_permlane32_swap_b32_e32 v218, v219
	s_cmp_eq_u32 s94, 0
	s_cbranch_scc0 .Lstg_mid4_l0
	s_waitcnt vmcnt(0)
	s_barrier
	s_mov_b32 m0, s92
	s_nop 0
	global_load_lds_dwordx4 v164, s[24:25]
	s_mov_b32 m0, s86
	s_nop 0
	global_load_lds_dwordx4 v170, s[26:27]
	s_add_u32 s24, s24, 0x3000
	s_addc_u32 s25, s25, 0
	s_add_u32 s26, s26, 64
	s_addc_u32 s27, s27, 0
.Lstg_mid4_l0:
	ds_read_b128 v[86:89], v194 offset:32768
	ds_read_b128 v[82:85], v193 offset:32768
	ds_read_b128 v[90:93], v193 offset:34816
	ds_read_b128 v[94:97], v194 offset:34816
	v_max_f32_e32 v182, v114, v115
	v_max_f32_e32 v183, v114, v114
	s_waitcnt lgkmcnt(0)
	v_mfma_f32_32x32x64_f8f6f4 v[2:17], v[130:137], v[82:89], v[2:17]
	v_max3_f32 v182, v182, v116, v117
	v_max3_f32 v182, v182, v118, v119
	v_max3_f32 v182, v182, v120, v121
	v_max3_f32 v182, v182, v122, v123
	v_max3_f32 v182, v182, v124, v125
	v_max3_f32 v182, v182, v126, v127
	v_max3_f32 v182, v182, v128, v129
	v_max3_f32 v182, v182, v98, v99
	v_mov_b32_e32 v220, 1.0
	v_mfma_f32_32x32x64_f8f6f4 v[50:65], v[130:137], v[90:97], v[50:65]
	ds_read_b128 v[82:85], v193 offset:36864
	ds_read_b128 v[90:93], v193 offset:38912
	ds_read_b128 v[86:89], v194 offset:36864
	ds_read_b128 v[94:97], v194 offset:38912
	s_waitcnt lgkmcnt(0)
	v_mfma_f32_32x32x64_f8f6f4 v[34:49], v[130:137], v[82:89], v[34:49]
	v_max3_f32 v82, v182, v100, v101
	v_max3_f32 v82, v82, v102, v103
	v_max3_f32 v82, v82, v104, v105
	v_max3_f32 v82, v82, v106, v107
	v_max3_f32 v82, v82, v108, v109
	v_max3_f32 v82, v82, v110, v111
	v_max3_f32 v82, v82, v112, v113
	v_mov_b32_e32 v83, v82
	s_nop 1
	v_permlane32_swap_b32_e32 v82, v83
	v_max_f32_e32 v82, v82, v83
	v_cmp_ge_f32_e32 vcc, s85, v82
	s_cmp_eq_u64 vcc, exec
	v_mfma_f32_32x32x64_f8f6f4 v[18:33], v[130:137], v[90:97], v[18:33]
	s_cbranch_scc0 .LBB0_935
	s_setprio 0
	s_branch .LBB0_922

; template <bool FIRST>
; __device__ __forceinline__ void partialSM(f32x16& p0, f32x16& p1, float& m_reg, f32x16& nm16, float& alpha) {
;   float pmax = p0[0];
; #pragma unroll
;   for (int r = 1; r < 16; ++r) pmax = fmaxf(pmax, p0[r]);
; #pragma unroll
;   for (int r = 0; r < 16; ++r) pmax = fmaxf(pmax, p1[r]);
;   { auto rr = __builtin_amdgcn_permlane32_swap(__float_as_uint(pmax), __float_as_uint(pmax), false, false);
;     pmax = fmaxf(__uint_as_float(rr[0]), __uint_as_float(rr[1])); }
;   if (!FIRST && __builtin_expect(__all(pmax <= THR2), 1)) { alpha = 1.f; }
;   else { const float d = FIRST ? pmax : fmaxf(pmax, 0.f);
;     alpha = FIRST ? 1.f : __builtin_amdgcn_exp2f(-d); m_reg += d;
;     const float nm = -m_reg;
; #pragma unroll
;     for (int r = 0; r < 16; ++r) { p0[r] -= d; p1[r] -= d; float t = nm16[r]; asm volatile("v_mov_b32 %0, %1" : "+v"(t) : "v"(nm)); nm16[r] = t; } }
; #pragma unroll
;   for (int r = 0; r < 16; ++r) p0[r] = __builtin_amdgcn_exp2f(p0[r]);
; }
; __device__ __forceinline__ void finishSM(f32x16& p0, f32x16& p1, float alpha, float& l_reg, v8i& pa) {
; #pragma unroll
;   for (int r = 0; r < 16; ++r) p1[r] = __builtin_amdgcn_exp2f(p1[r]);
;   float ps = 0;
; #pragma unroll
;   for (int r = 0; r < 16; ++r) ps += p0[r];
; #pragma unroll
;   for (int r = 0; r < 16; ++r) ps += p1[r];
;   { auto rr = __builtin_amdgcn_permlane32_swap(__float_as_uint(ps), __float_as_uint(ps), false, false);
;     ps = __uint_as_float(rr[0]) + __uint_as_float(rr[1]); }
;   l_reg = l_reg * alpha + ps;
; #pragma unroll
;   for (int q = 0; q < 4; ++q) { int w0 = pa[q], w1 = pa[4 + q];
;     w0 = __builtin_amdgcn_cvt_pk_fp8_f32(p0[4 * q], p0[4 * q + 1], w0, false); w0 = __builtin_amdgcn_cvt_pk_fp8_f32(p0[4 * q + 2], p0[4 * q + 3], w0, true);
;     w1 = __builtin_amdgcn_cvt_pk_fp8_f32(p1[4 * q], p1[4 * q + 1], w1, false); w1 = __builtin_amdgcn_cvt_pk_fp8_f32(p1[4 * q + 2], p1[4 * q + 3], w1, true);
;     pa[q] = w0; pa[4 + q] = w1; }
; }
; __device__ __forceinline__ void qkt(f32x16& p0, f32x16& p1, const char* Ks, const v8i* qr, int r32, int hi, const f32x16& nm16) {
; #pragma unroll
;   for (int s = 0; s < 3; ++s) { const int c0 = 4 * s + 2 * hi;
;     const v8i a0 = __builtin_shufflevector(*reinterpret_cast<const v4i*>(Ks + k8_off(r32, c0)), *reinterpret_cast<const v4i*>(Ks + k8_off(r32, c0 + 1)), 0, 1, 2, 3, 4, 5, 6, 7);
.Lstg_end4_l0:
	v_exp_f32_e32 v176, v114
	v_exp_f32_e32 v177, v115
	v_exp_f32_e32 v178, v116
	v_exp_f32_e32 v179, v117
	v_exp_f32_e32 v180, v118
	v_exp_f32_e32 v181, v119
	v_exp_f32_e32 v182, v120
	v_exp_f32_e32 v183, v121
	v_exp_f32_e32 v184, v122
	v_exp_f32_e32 v185, v123
	v_exp_f32_e32 v221, v124
	v_exp_f32_e32 v238, v125
	v_exp_f32_e32 v239, v126
	v_exp_f32_e32 v240, v127
	v_exp_f32_e32 v241, v128
	v_exp_f32_e32 v242, v129
	ds_read_b128 v[82:85], v196 offset:8192
	ds_read_b128 v[86:89], v197 offset:8192
	ds_read_b128 v[222:225], v196 offset:14336
	ds_read_b128 v[226:229], v197 offset:14336
	v_exp_f32_e32 v100, v100
	v_exp_f32_e32 v101, v101
	s_waitcnt lgkmcnt(0)
	v_mfma_f32_32x32x64_f8f6f4 v[114:129], v[82:89], v[138:145], v[66:81]
	v_exp_f32_e32 v102, v102
	v_exp_f32_e32 v103, v103
	v_exp_f32_e32 v104, v104
	v_exp_f32_e32 v105, v105
	v_exp_f32_e32 v106, v106
	v_exp_f32_e32 v107, v107
	v_exp_f32_e32 v108, v108
	v_exp_f32_e32 v110, v110
	v_exp_f32_e32 v111, v111
	v_exp_f32_e32 v109, v109
	v_exp_f32_e32 v112, v112
	v_exp_f32_e32 v113, v113
	v_cvt_pk_fp8_f32 v130, v176, v177
	v_cvt_pk_fp8_f32 v131, v180, v181
	v_cvt_pk_fp8_f32 v135, v102, v103
	v_mfma_f32_32x32x64_f8f6f4 v[82:97], v[222:229], v[138:145], v[66:81]
	ds_read_b128 v[222:225], v198 offset:8192
	ds_read_b128 v[226:229], v199 offset:8192
	ds_read_b128 v[230:233], v198 offset:14336
	ds_read_b128 v[234:237], v199 offset:14336
	s_setprio 1
	v_cvt_pk_fp8_f32 v132, v184, v185
	v_cvt_pk_fp8_f32 v136, v106, v107
	v_cvt_pk_fp8_f32 v133, v239, v240
	v_cvt_pk_fp8_f32 v137, v110, v111
	v_cvt_pk_fp8_f32 v130, v178, v179 op_sel:[0,0,1]
	v_cvt_pk_fp8_f32 v131, v182, v183 op_sel:[0,0,1]
	v_cvt_pk_fp8_f32 v135, v104, v105 op_sel:[0,0,1]
	v_cvt_pk_fp8_f32 v132, v221, v238 op_sel:[0,0,1]
	v_cvt_pk_fp8_f32 v136, v108, v109 op_sel:[0,0,1]
	v_cvt_pk_fp8_f32 v133, v241, v242 op_sel:[0,0,1]
	v_cvt_pk_fp8_f32 v137, v112, v113 op_sel:[0,0,1]
	s_waitcnt lgkmcnt(0)
	v_mfma_f32_32x32x64_f8f6f4 v[114:129], v[222:229], v[146:153], v[114:129]
	v_mfma_f32_32x32x64_f8f6f4 v[82:97], v[230:237], v[146:153], v[82:97]
	ds_read_b128 v[222:225], v200 offset:8192
	ds_read_b128 v[226:229], v201 offset:8192
	ds_read_b128 v[230:233], v200 offset:14336
	ds_read_b128 v[234:237], v201 offset:14336
	s_waitcnt lgkmcnt(0)
	v_mfma_f32_32x32x64_f8f6f4 v[114:129], v[222:229], v[154:161], v[114:129]
	v_exp_f32_e32 v222, v98
	v_add_f32_e32 v98, 0, v176
	v_add_f32_e32 v98, v177, v98
	v_add_f32_e32 v98, v178, v98
	v_add_f32_e32 v98, v179, v98
	v_add_f32_e32 v98, v180, v98
	v_add_f32_e32 v98, v181, v98
	v_add_f32_e32 v98, v182, v98
	v_add_f32_e32 v98, v183, v98
	v_add_f32_e32 v98, v184, v98
	v_add_f32_e32 v98, v185, v98
	v_add_f32_e32 v98, v221, v98
	v_add_f32_e32 v98, v238, v98
	v_add_f32_e32 v98, v239, v98
	v_exp_f32_e32 v223, v99
	v_add_f32_e32 v98, v240, v98
	v_add_f32_e32 v98, v241, v98
	v_add_f32_e32 v98, v242, v98
	v_add_f32_e32 v98, v222, v98
	v_add_f32_e32 v98, v223, v98
	v_mfma_f32_32x32x64_f8f6f4 v[82:97], v[230:237], v[154:161], v[82:97]
	v_add_f32_e32 v98, v100, v98
	v_add_f32_e32 v98, v101, v98
	v_add_f32_e32 v98, v102, v98
	v_add_f32_e32 v98, v103, v98
	v_add_f32_e32 v98, v104, v98
	v_add_f32_e32 v98, v105, v98
	v_add_f32_e32 v98, v106, v98
	v_add_f32_e32 v98, v107, v98
	v_add_f32_e32 v98, v108, v98
	v_cvt_pk_fp8_f32 v134, v222, v223
	v_add_f32_e32 v98, v109, v98
	v_add_f32_e32 v98, v110, v98
	v_add_f32_e32 v98, v111, v98
	v_add_f32_e32 v98, v112, v98
	v_cvt_pk_fp8_f32 v134, v100, v101 op_sel:[0,0,1]
	v_add_f32_e32 v98, v113, v98
	v_mov_b32_e32 v99, v98
	s_nop 1
	v_permlane32_swap_b32_e32 v98, v99
	s_cmp_eq_u32 s94, 0
	s_cbranch_scc0 .Lstg_mid5_l0
	s_waitcnt vmcnt(0)
	s_barrier
	s_cmp_lt_i32 s9, 49
	s_cbranch_scc0 .Lstg_mid5_l0
	s_mov_b32 m0, s90
	s_nop 0
	global_load_lds_dwordx4 v164, s[24:25]
	s_mov_b32 m0, s88
	s_nop 0
	global_load_lds_dwordx4 v170, s[26:27]
	s_add_u32 s24, s24, 0x3000
	s_addc_u32 s25, s25, 0
	s_add_u32 s26, s26, 64
	s_addc_u32 s27, s27, 0
.Lstg_mid5_l0:
	ds_read_b128 v[104:107], v194 offset:40960
	ds_read_b128 v[100:103], v193 offset:40960
	ds_read_b128 v[222:225], v193 offset:43008
	ds_read_b128 v[226:229], v194 offset:43008
	v_max_f32_e32 v108, v114, v115
	v_max_f32_e32 v109, v114, v114
	s_waitcnt lgkmcnt(0)
	v_mfma_f32_32x32x64_f8f6f4 v[2:17], v[130:137], v[100:107], v[2:17]
	v_max3_f32 v108, v108, v116, v117
	v_max3_f32 v108, v108, v118, v119
	v_max3_f32 v108, v108, v120, v121
	v_max3_f32 v108, v108, v122, v123
	v_max3_f32 v108, v108, v124, v125
	v_max3_f32 v108, v108, v126, v127
	v_max3_f32 v108, v108, v128, v129
	v_max3_f32 v108, v108, v82, v83
	v_mov_b32_e32 v176, 1.0
	v_mfma_f32_32x32x64_f8f6f4 v[50:65], v[130:137], v[222:229], v[50:65]
	ds_read_b128 v[100:103], v193 offset:45056
	ds_read_b128 v[222:225], v193 offset:47104
	ds_read_b128 v[104:107], v194 offset:45056
	ds_read_b128 v[226:229], v194 offset:47104
	s_waitcnt lgkmcnt(0)
	v_mfma_f32_32x32x64_f8f6f4 v[34:49], v[130:137], v[100:107], v[34:49]
	v_max3_f32 v100, v108, v84, v85
	v_max3_f32 v100, v100, v86, v87
	v_max3_f32 v100, v100, v88, v89
	v_max3_f32 v100, v100, v90, v91
	v_max3_f32 v100, v100, v92, v93
	v_max3_f32 v100, v100, v94, v95
	v_max3_f32 v100, v100, v96, v97
	v_mov_b32_e32 v101, v100
	s_nop 1
	v_permlane32_swap_b32_e32 v100, v101
	v_max_f32_e32 v100, v100, v101
	v_cmp_ge_f32_e32 vcc, s85, v100
	s_cmp_eq_u64 vcc, exec
	v_mfma_f32_32x32x64_f8f6f4 v[18:33], v[130:137], v[222:229], v[18:33]
	s_cbranch_scc0 .LBB0_936
	s_setprio 0
	s_branch .LBB0_929

; template <bool FIRST>
; __device__ __forceinline__ void partialSM(f32x16& p0, f32x16& p1, float& m_reg, f32x16& nm16, float& alpha) {
;   float pmax = p0[0];
; #pragma unroll
;   for (int r = 1; r < 16; ++r) pmax = fmaxf(pmax, p0[r]);
; #pragma unroll
;   for (int r = 0; r < 16; ++r) pmax = fmaxf(pmax, p1[r]);
;   { auto rr = __builtin_amdgcn_permlane32_swap(__float_as_uint(pmax), __float_as_uint(pmax), false, false);
;     pmax = fmaxf(__uint_as_float(rr[0]), __uint_as_float(rr[1])); }
;   if (!FIRST && __builtin_expect(__all(pmax <= THR2), 1)) { alpha = 1.f; }
;   else { const float d = FIRST ? pmax : fmaxf(pmax, 0.f);
;     alpha = FIRST ? 1.f : __builtin_amdgcn_exp2f(-d); m_reg += d;
;     const float nm = -m_reg;
; #pragma unroll
;     for (int r = 0; r < 16; ++r) { p0[r] -= d; p1[r] -= d; float t = nm16[r]; asm volatile("v_mov_b32 %0, %1" : "+v"(t) : "v"(nm)); nm16[r] = t; } }
; #pragma unroll
;   for (int r = 0; r < 16; ++r) p0[r] = __builtin_amdgcn_exp2f(p0[r]);
; }
; __device__ __forceinline__ void finishSM(f32x16& p0, f32x16& p1, float alpha, float& l_reg, v8i& pa) {
; #pragma unroll
;   for (int r = 0; r < 16; ++r) p1[r] = __builtin_amdgcn_exp2f(p1[r]);
;   float ps = 0;
; #pragma unroll
;   for (int r = 0; r < 16; ++r) ps += p0[r];
; #pragma unroll
;   for (int r = 0; r < 16; ++r) ps += p1[r];
;   { auto rr = __builtin_amdgcn_permlane32_swap(__float_as_uint(ps), __float_as_uint(ps), false, false);
;     ps = __uint_as_float(rr[0]) + __uint_as_float(rr[1]); }
;   l_reg = l_reg * alpha + ps;
; #pragma unroll
;   for (int q = 0; q < 4; ++q) { int w0 = pa[q], w1 = pa[4 + q];
;     w0 = __builtin_amdgcn_cvt_pk_fp8_f32(p0[4 * q], p0[4 * q + 1], w0, false); w0 = __builtin_amdgcn_cvt_pk_fp8_f32(p0[4 * q + 2], p0[4 * q + 3], w0, true);
;     w1 = __builtin_amdgcn_cvt_pk_fp8_f32(p1[4 * q], p1[4 * q + 1], w1, false); w1 = __builtin_amdgcn_cvt_pk_fp8_f32(p1[4 * q + 2], p1[4 * q + 3], w1, true);
;     pa[q] = w0; pa[4 + q] = w1; }
; }
; __device__ __forceinline__ void qkt(f32x16& p0, f32x16& p1, const char* Ks, const v8i* qr, int r32, int hi, const f32x16& nm16) {
; #pragma unroll
;   for (int s = 0; s < 3; ++s) { const int c0 = 4 * s + 2 * hi;
;     const v8i a0 = __builtin_shufflevector(*reinterpret_cast<const v4i*>(Ks + k8_off(r32, c0)), *reinterpret_cast<const v4i*>(Ks + k8_off(r32, c0 + 1)), 0, 1, 2, 3, 4, 5, 6, 7);
.Lstg_end4_l1:
	v_exp_f32_e32 v176, v114
	v_exp_f32_e32 v177, v115
	v_exp_f32_e32 v178, v116
	v_exp_f32_e32 v179, v117
	v_exp_f32_e32 v180, v118
	v_exp_f32_e32 v181, v119
	v_exp_f32_e32 v182, v120
	v_exp_f32_e32 v183, v121
	v_exp_f32_e32 v184, v122
	v_exp_f32_e32 v185, v123
	v_exp_f32_e32 v221, v124
	v_exp_f32_e32 v238, v125
	v_exp_f32_e32 v239, v126
	v_exp_f32_e32 v240, v127
	v_exp_f32_e32 v241, v128
	v_exp_f32_e32 v242, v129
	ds_read_b128 v[82:85], v196 offset:8192
	ds_read_b128 v[86:89], v197 offset:8192
	ds_read_b128 v[222:225], v196 offset:14336
	ds_read_b128 v[226:229], v197 offset:14336
	v_exp_f32_e32 v100, v100
	v_exp_f32_e32 v101, v101
	s_waitcnt lgkmcnt(0)
	v_mfma_f32_32x32x64_f8f6f4 v[114:129], v[82:89], v[138:145], v[66:81]
	v_exp_f32_e32 v102, v102
	v_exp_f32_e32 v103, v103
	v_exp_f32_e32 v104, v104
	v_exp_f32_e32 v105, v105
	v_exp_f32_e32 v106, v106
	v_exp_f32_e32 v107, v107
	v_exp_f32_e32 v108, v108
	v_exp_f32_e32 v110, v110
	v_exp_f32_e32 v111, v111
	v_exp_f32_e32 v109, v109
	v_exp_f32_e32 v112, v112
	v_exp_f32_e32 v113, v113
	v_cvt_pk_fp8_f32 v130, v176, v177
	v_cvt_pk_fp8_f32 v131, v180, v181
	v_cvt_pk_fp8_f32 v135, v102, v103
	v_mfma_f32_32x32x64_f8f6f4 v[82:97], v[222:229], v[138:145], v[66:81]
	ds_read_b128 v[222:225], v198 offset:8192
	ds_read_b128 v[226:229], v199 offset:8192
	ds_read_b128 v[230:233], v198 offset:14336
	ds_read_b128 v[234:237], v199 offset:14336
	s_setprio 1
	v_cvt_pk_fp8_f32 v132, v184, v185
	v_cvt_pk_fp8_f32 v136, v106, v107
	v_cvt_pk_fp8_f32 v133, v239, v240
	v_cvt_pk_fp8_f32 v137, v110, v111
	v_cvt_pk_fp8_f32 v130, v178, v179 op_sel:[0,0,1]
	v_cvt_pk_fp8_f32 v131, v182, v183 op_sel:[0,0,1]
	v_cvt_pk_fp8_f32 v135, v104, v105 op_sel:[0,0,1]
	v_cvt_pk_fp8_f32 v132, v221, v238 op_sel:[0,0,1]
	v_cvt_pk_fp8_f32 v136, v108, v109 op_sel:[0,0,1]
	v_cvt_pk_fp8_f32 v133, v241, v242 op_sel:[0,0,1]
	v_cvt_pk_fp8_f32 v137, v112, v113 op_sel:[0,0,1]
	s_waitcnt lgkmcnt(0)
	v_mfma_f32_32x32x64_f8f6f4 v[114:129], v[222:229], v[146:153], v[114:129]
	v_mfma_f32_32x32x64_f8f6f4 v[82:97], v[230:237], v[146:153], v[82:97]
	ds_read_b128 v[222:225], v200 offset:8192
	ds_read_b128 v[226:229], v201 offset:8192
	ds_read_b128 v[230:233], v200 offset:14336
	ds_read_b128 v[234:237], v201 offset:14336
	s_waitcnt lgkmcnt(0)
	v_mfma_f32_32x32x64_f8f6f4 v[114:129], v[222:229], v[154:161], v[114:129]
	v_exp_f32_e32 v222, v98
	v_add_f32_e32 v98, 0, v176
	v_add_f32_e32 v98, v177, v98
	v_add_f32_e32 v98, v178, v98
	v_add_f32_e32 v98, v179, v98
	v_add_f32_e32 v98, v180, v98
	v_add_f32_e32 v98, v181, v98
	v_add_f32_e32 v98, v182, v98
	v_add_f32_e32 v98, v183, v98
	v_add_f32_e32 v98, v184, v98
	v_add_f32_e32 v98, v185, v98
	v_add_f32_e32 v98, v221, v98
	v_add_f32_e32 v98, v238, v98
	v_add_f32_e32 v98, v239, v98
	v_exp_f32_e32 v223, v99
	v_add_f32_e32 v98, v240, v98
	v_add_f32_e32 v98, v241, v98
	v_add_f32_e32 v98, v242, v98
	v_add_f32_e32 v98, v222, v98
	v_add_f32_e32 v98, v223, v98
	v_mfma_f32_32x32x64_f8f6f4 v[82:97], v[230:237], v[154:161], v[82:97]
	v_add_f32_e32 v98, v100, v98
	v_add_f32_e32 v98, v101, v98
	v_add_f32_e32 v98, v102, v98
	v_add_f32_e32 v98, v103, v98
	v_add_f32_e32 v98, v104, v98
	v_add_f32_e32 v98, v105, v98
	v_add_f32_e32 v98, v106, v98
	v_add_f32_e32 v98, v107, v98
	v_add_f32_e32 v98, v108, v98
	v_cvt_pk_fp8_f32 v134, v222, v223
	v_add_f32_e32 v98, v109, v98
	v_add_f32_e32 v98, v110, v98
	v_add_f32_e32 v98, v111, v98
	v_add_f32_e32 v98, v112, v98
	v_cvt_pk_fp8_f32 v134, v100, v101 op_sel:[0,0,1]
	v_add_f32_e32 v98, v113, v98
	v_mov_b32_e32 v99, v98
	s_nop 1
	v_permlane32_swap_b32_e32 v98, v99
	s_cmp_eq_u32 s94, 0
	s_cbranch_scc0 .Lstg_mid5_l1
	s_waitcnt vmcnt(0)
	s_barrier
	s_cmp_lt_i32 s8, 49
	s_cbranch_scc0 .Lstg_mid5_l1
	s_mov_b32 m0, s90
	s_nop 0
	global_load_lds_dwordx4 v164, s[24:25]
	s_mov_b32 m0, s88
	s_nop 0
	global_load_lds_dwordx4 v170, s[26:27]
	s_add_u32 s24, s24, 0x3000
	s_addc_u32 s25, s25, 0
	s_add_u32 s26, s26, 64
	s_addc_u32 s27, s27, 0
